# gathered MoBA units: the second K/V stage is requested in the unit prologue (both ring slots are free there) instead of at the top of the first loop pass
# baseline (speedup 1.0000x reference)
; __device__ __forceinline__ unsigned ld_sc1(const unsigned* p) { return __hip_atomic_load(p, __ATOMIC_RELAXED, __HIP_MEMORY_SCOPE_AGENT); }
; template <int mode> __device__ __forceinline__ void attn_unit(const AttnArgs& A, const int b, const int h, const int sub, char* shm, const int wave_) {
;     ...
;     if (mode == 3) { gk = sub >> 4; const int c = sub & 15; const int li = (b * 5 + (h - 6)) * 15 + gk;
;         gcnt = __builtin_amdgcn_readfirstlane((int)ld_sc1(A.mcnt + li));
;         if (c * 256 >= gcnt) return;
;         const int gi = c * 256 + wid * 32 + r32; gvalid = gi < gcnt; wvalid = (c * 256 + wid * 32) < gcnt;
;         gent = ld_sc1(A.mlist + (size_t)li * MLCAP + (gvalid ? gi : 0)); qb = 0; }
;     const size_t rowbase = (size_t)b * SEQ + res; const int q0 = qb * 256;
;     const bf16* Qp = A.qkv + (rowbase + (size_t)dil * ((mode == 3) ? (int)(gent & 4095u) : (q0 + wid * 32 + r32))) * QS + h * 128;
;     const bf16* Kh = A.qkv + rowbase * QS + 2048 + h * 128;
;     const bf16* Vh = A.qkv + rowbase * QS + 4096 + h * 128;
;     const size_t rstep = (size_t)dil * QS;
;     char* V_lds = shm + L_V; char* K_lds = shm + L_K;
;     float* wsf = (float*)(shm + L_WS) + wid * 64; float* li_l = wsf; float* al_l = wsf + 32;
;     int* TL = (int*)(shm + L_TL); int* FLG = (int*)(shm + L_FLG); unsigned* MSK = (unsigned*)(shm + L_MSK); float* KM = (float*)(shm + L_KM);
;     char* qf = shm + L_Q + wid * 8192 + lane * 16;
;     const int qw0 = q0 + wid * 32;
;     const int pos = qw0 + r32;
;     const int vb0 = (int)(uintptr_t)V_lds + v_rd_base(lane);
;     unsigned koffb[2], voffb[2];
; #pragma unroll
;     for (int i = 0; i < 2; ++i) { const int Lb = (2 * wid + i) * 1024 + lane * 16;
;         const int rowk = Lb >> 8, ck = ((Lb >> 4) & 15) ^ (rowk & 7);
;         koffb[i] = (unsigned)(((size_t)rowk * rstep + ck * 8) * 2);
;         const int sub_ = Lb >> 9, win_ = Lb & 511, kk = (sub_ >> 2) * 8 + (win_ >> 6), kv = (kk & ~0xC) | ((kk & 4) << 1) | ((kk & 8) >> 1), cc = (sub_ & 3) * 4 + ((win_ & 63) >> 4);
;         voffb[i] = (unsigned)(((size_t)kv * rstep + cc * 8) * 2); }
;     typedef __attribute__((address_space(3))) unsigned lds_u32;
;     lds_u32* const Kdst = (lds_u32*)(K_lds + wid * 2048); lds_u32* const Vdst = (lds_u32*)(V_lds + wid * 2048);
;     ...
;     { const int kf_ = ((mode == 3) ? gk * 256 : q0) + 192; TDMA(kf_, 0); }
;     bf16x8 qr[8];
; #pragma unroll
.LBB0_516:
	s_bfe_u32 s1, s26, 0x1000b
	s_bfe_u32 s19, s26, 0x30008
	s_mul_i32 s14, s1, 5
	s_add_i32 s14, s14, s19
	s_bfe_u32 s0, s26, 0x40004
	s_mul_i32 s14, s14, 15
	s_add_i32 s14, s14, s0
	v_mbcnt_lo_u32_b32 v0, -1, 0
	v_mbcnt_hi_u32_b32 v0, -1, v0
	s_lshl_b32 s15, s14, 2
	v_readlane_b32 s16, v255, 10
	s_waitcnt vmcnt(18)
	v_add_u32_e32 v119, s94, v0
	v_mov_b32_e32 v0, s15
	v_readlane_b32 s17, v255, 11
	s_lshl_b32 s15, s26, 8
	s_and_b32 s25, s15, 0xf00
	s_nop 2
	global_load_dword v0, v0, s[16:17] sc1
	v_readlane_b32 s22, v252, 37
	v_and_b32_e32 v120, 31, v119
	s_mul_i32 s98, s14, 0x3c00
	v_readlane_b32 s16, v255, 8
	v_readlane_b32 s17, v255, 9
	s_add_i32 s22, s25, s22
	v_or_b32_e32 v116, s22, v120
	v_mov_b32_e32 v117, v1
	s_add_u32 s98, s16, s98
	s_addc_u32 s99, s17, 0
	v_lshl_add_u64 v[2:3], v[116:117], 2, s[98:99]
	global_load_dword v122, v[2:3], off sc1
	global_load_dword v117, v1, s[98:99] sc1
	s_waitcnt vmcnt(2)
	v_readfirstlane_b32 s24, v0
	s_cmp_ge_i32 s25, s24
	s_cbranch_scc1 .LBB0_666
	v_readlane_b32 s15, v252, 37
	v_and_b32_e32 v120, 31, v119
	s_add_i32 s25, s25, s15
	s_add_i32 s22, s19, 6
	v_or_b32_e32 v0, s25, v120
	s_mulk_i32 s14, 0x3c00
	v_readlane_b32 s16, v255, 8
	v_cmp_gt_i32_e64 s[40:41], s24, v0
	v_readlane_b32 s17, v255, 9
	s_add_u32 s14, s16, s14
	s_addc_u32 s15, s17, 0
	v_cndmask_b32_e64 v0, 0, v0, s[40:41]
	s_lshl_b32 s14, s1, 12
	s_lshl_b32 s18, s22, 7
	s_mul_i32 s1, s1, 0x3000000
	s_add_u32 s1, s38, s1
	s_addc_u32 s15, s39, 0
	s_lshl_b32 s30, s22, 8
	s_add_u32 s1, s1, s30
	v_and_b32_e32 v4, 63, v119
	s_addc_u32 s27, s15, 0
	v_lshlrev_b32_e32 v6, 4, v4
	v_readlane_b32 s23, v252, 28
	v_lshrrev_b32_e32 v8, 1, v119
	s_add_u32 s15, s1, 0x1000
	v_or_b32_e32 v2, s23, v6
	v_bfe_u32 v7, v119, 2, 2
	v_and_b32_e32 v8, 8, v8
	v_readlane_b32 s23, v252, 13
	s_addc_u32 s22, s27, 0
	v_and_b32_e32 v3, 15, v119
	v_or3_b32 v7, v7, v8, s23
	s_add_u32 s23, s1, 0x2000
	v_ashrrev_i32_e32 v9, 8, v2
	s_addc_u32 s27, s27, 0
	s_lshl_b32 s0, s0, 8
	v_bitop3_b32 v10, v9, v3, 3 bitop3:0x6c
	v_mul_i32_i24_e32 v9, 0x3000, v9
	s_or_b32 s28, s0, 0xc0
	v_and_b32_e32 v8, 3, v119
	v_lshl_or_b32 v125, v10, 4, v9
	v_lshrrev_b32_e32 v9, 3, v119
	s_mul_i32 s29, s28, 0x3000
	v_mul_lo_u32 v7, v7, s70
	v_and_or_b32 v9, v9, 4, v8
	v_or_b32_e32 v2, 0x400, v2
	s_add_u32 s0, s15, s29
	v_lshl_or_b32 v126, v9, 4, v7
	v_ashrrev_i32_e32 v9, 8, v2
	v_lshrrev_b32_e32 v2, 7, v2
	s_addc_u32 s1, s22, 0
	v_bitop3_b32 v3, v9, v3, 7 bitop3:0x6c
	v_mul_i32_i24_e32 v9, 0x3000, v9
	v_and_or_b32 v2, v2, 12, v8
	s_add_u32 s34, s23, s29
	v_bfe_u32 v5, v119, 5, 1
	v_lshl_or_b32 v127, v3, 4, v9
	v_lshl_or_b32 v128, v2, 4, v7
	s_mov_b32 s31, s90
	s_addc_u32 s35, s27, 0
	v_mov_b32_e32 v7, v125
	s_add_i32 m0, s2, 0x8000
	v_lshlrev_b32_e32 v114, 4, v5
	v_mov_b32_e32 v115, v1
	v_cmp_gt_i32_e32 vcc, 4, v119
	s_waitcnt vmcnt(0)
	v_cndmask_b32_e64 v122, v117, v122, s[40:41]
	v_and_b32_e32 v121, 0xfff, v122
	v_or_b32_e32 v0, s14, v121
	v_mul_u32_u24_e32 v0, 0x1800, v0
	v_lshlrev_b32_e32 v0, 1, v0
	v_lshl_add_u64 v[2:3], s[38:39], 0, v[0:1]
	v_mov_b32_e32 v0, v126
	v_lshl_add_u64 v[2:3], v[2:3], 0, s[30:31]
	global_load_lds_dwordx4 v7, s[0:1]
	s_mov_b32 m0, s2
	v_mov_b32_e32 v7, v127
	global_load_lds_dwordx4 v0, s[34:35]
	v_mov_b32_e32 v0, v128
	v_lshl_add_u64 v[2:3], v[2:3], 0, v[114:115]
	global_load_dwordx4 v[8:11], v[2:3], off
	global_load_dwordx4 v[16:19], v[2:3], off offset:32
	global_load_dwordx4 v[20:23], v[2:3], off offset:64
	global_load_dwordx4 v[24:27], v[2:3], off offset:96
	global_load_dwordx4 v[28:31], v[2:3], off offset:128
	global_load_dwordx4 v[32:35], v[2:3], off offset:160
	global_load_dwordx4 v[36:39], v[2:3], off offset:192
	global_load_dwordx4 v[40:43], v[2:3], off offset:224
	s_add_i32 m0, s2, 0x8400
	s_nop 0
	global_load_lds_dwordx4 v7, s[0:1]
	s_add_u32 s98, s0, 0xfff40000
	s_addc_u32 s99, s1, -1
	v_readlane_b32 s0, v252, 15
	s_add_i32 m0, s2, 0x400
	s_nop 0
	v_add_u32_e32 v123, s0, v6
	global_load_lds_dwordx4 v0, s[34:35]
	s_add_i32 m0, s2, 0xc000
	s_nop 0
	global_load_lds_dwordx4 v125, s[98:99]
	s_add_i32 m0, s2, 0xc400
	s_nop 0
	global_load_lds_dwordx4 v127, s[98:99]
	s_add_u32 s98, s34, 0xfff40000
	s_addc_u32 s99, s35, -1
	s_add_i32 m0, s2, 0x4000
	s_nop 0
	global_load_lds_dwordx4 v126, s[98:99]
	s_add_i32 m0, s2, 0x4400
	s_nop 0
	global_load_lds_dwordx4 v128, s[98:99]
	s_waitcnt vmcnt(4)
	ds_write_b128 v123, v[8:11]
	ds_write_b128 v123, v[16:19] offset:1024
	ds_write_b128 v123, v[20:23] offset:2048
	ds_write_b128 v123, v[24:27] offset:3072
	ds_write_b128 v123, v[28:31] offset:4096
	ds_write_b128 v123, v[32:35] offset:5120
	ds_write_b128 v123, v[36:39] offset:6144
	ds_write_b128 v123, v[40:43] offset:7168
	s_and_saveexec_b64 s[0:1], vcc
	v_lshl_add_u32 v0, v119, 2, 0
	v_lshlrev_b32_e32 v2, 6, v119
	v_add_u32_e32 v0, 0x20800, v0
	v_sub_u32_e32 v2, s28, v2
	ds_write_b32 v0, v2
	s_or_b64 exec, exec, s[0:1]
	s_cmp_lt_i32 s25, s24
	s_cselect_b64 s[24:25], -1, 0
	s_lshl_b32 s0, s19, 3
	s_sub_i32 s0, 0xffffffc8, s0
	v_cvt_f32_i32_e32 v0, s0
	s_mov_b32 s28, 0x41300000
	v_lshlrev_b32_e32 v5, 2, v5
	v_and_b32_e32 v22, 0xc0, v6
	v_div_scale_f32 v2, s[0:1], s28, s28, v0
	v_rcp_f32_e32 v3, v2
	v_div_scale_f32 v7, vcc, v0, s28, v0
	v_or_b32_e32 v6, 2, v5
	v_fma_f32 v8, -v2, v3, 1.0
	v_fmac_f32_e32 v3, v8, v3
	v_mul_f32_e32 v8, v7, v3
	v_fma_f32 v9, -v2, v8, v7
	v_fmac_f32_e32 v8, v9, v3
	v_fma_f32 v2, -v2, v8, v7
	v_div_fmas_f32 v2, v2, v3, v8
	v_div_fixup_f32 v0, v2, s28, v0
	v_exp_f32_e32 v0, v0
	v_or_b32_e32 v2, 3, v5
	v_cvt_f32_ubyte0_e32 v3, v2
	v_cvt_f32_ubyte0_e32 v2, v6
	v_mul_f32_e32 v118, 0x3fb8aa3b, v0
	v_lshlrev_b32_e32 v21, 1, v4
	v_or_b32_e32 v0, 1, v5
	v_pk_mul_f32 v[68:69], v[118:119], v[2:3] op_sel_hi:[0,1]
	v_mov_b32_e32 v116, 0xf149f2ca
	v_mov_b32_e32 v117, v1
	v_mov_b32_e32 v2, v1
	v_lshlrev_b32_e32 v20, 3, v4
	v_cvt_f32_ubyte0_e32 v19, v0
	v_and_b32_e32 v0, 32, v21
	s_waitcnt lgkmcnt(0)
	s_barrier
; #define tid (tid_of(wave))
; template <int mode> __device__ __forceinline__ void attn_unit(const AttnArgs& A, const int b, const int h, const int sub, char* shm, const int wave_) {
;     ...
;     const float sl = (mode == 2) ? 0.f : __builtin_amdgcn_exp2f(-8.0f * (float)(h + 1) / 11.0f) * 1.4426950408889634f * (float)dil;
;     f32x16 binit;
; #pragma unroll
;     for (int r = 0; r < 16; ++r) binit[r] = sl * (float)((r & 3) + 8 * (r >> 2) + 4 * hi);
;     const float sl32 = 32.f * sl;
;     int NT = 0;
;     if (mode == 1) { NT = 4; if (tid < 4) TL[tid] = q0 + 192 - 64 * tid; }
;     else if (mode == 3) { NT = 4; if (tid < 4) TL[tid] = gk * 256 + 192 - 64 * tid; }
;     else if (mode == 0) {
;         const int lo = q0 >= 128 ? q0 - 128 : 0; NT = (q0 + 256 - lo) / 64;
;         if (tid < NT) TL[NT - 1 - tid] = lo + 64 * tid;
;     } else {
;         NT = (q0 + 256) / 64;
;         if (tid < NT) TL[tid] = q0 + 192 - 64 * tid;
;     }
;     __syncthreads();
;     float m_reg = -1e30f, l_reg = 0.f, carry = 0.f; asm volatile("" : "+v"(m_reg), "+v"(l_reg), "+v"(carry));
;     f32x16 o[4];
; #pragma unroll
;     for (int d0 = 0; d0 < 4; ++d0) o[d0] = f32x16{};
;     bool wdone = false;
	s_movk_i32 s0, 0x118
	v_or_b32_e32 v8, 8, v5
	v_or_b32_e32 v10, 10, v5
	v_or_b32_e32 v12, 16, v5
	v_or_b32_e32 v14, 18, v5
	v_or_b32_e32 v15, 25, v5
	v_or_b32_e32 v16, 24, v5
	v_and_or_b32 v0, v20, s0, v0
	v_lshlrev_b32_e32 v2, 4, v120
	s_movk_i32 s0, 0x70
	v_or_b32_e32 v7, 9, v5
	v_or_b32_e32 v9, 11, v5
	v_or_b32_e32 v11, 17, v5
	v_or_b32_e32 v13, 19, v5
	v_or_b32_e32 v18, 26, v5
	v_cvt_f32_ubyte0_e32 v6, v8
	v_cvt_f32_ubyte0_e32 v8, v10
	v_cvt_f32_ubyte0_e32 v10, v12
	v_cvt_f32_ubyte0_e32 v12, v14
	v_cvt_f32_ubyte0_e32 v15, v15
	v_cvt_f32_ubyte0_e32 v14, v16
	v_and_b32_e32 v3, 0x70, v2
	v_bitop3_b32 v135, v114, v2, s0 bitop3:0x78
	s_movk_i32 s0, 0x60
	s_cmp_lg_u32 0, -1
	v_or_b32_e32 v17, 27, v5
	v_cvt_f32_ubyte0_e32 v7, v7
	v_cvt_f32_ubyte0_e32 v9, v9
	v_cvt_f32_ubyte0_e32 v11, v11
	v_cvt_f32_ubyte0_e32 v13, v13
	v_cvt_f32_ubyte0_e32 v16, v18
	v_cvt_f32_ubyte0_e32 v18, v5
	v_pk_mul_f32 v[78:79], v[118:119], v[14:15] op_sel_hi:[0,1]
	v_bitop3_b32 v131, v114, v3, s0 bitop3:0x36
	s_cselect_b32 s0, 0, 0
	v_mov_b32_e32 v14, v1
	v_mov_b32_e32 v15, v1
	v_cvt_f32_ubyte0_e32 v17, v17
	v_pk_mul_f32 v[76:77], v[118:119], v[12:13] op_sel_hi:[0,1]
	v_pk_mul_f32 v[74:75], v[118:119], v[10:11] op_sel_hi:[0,1]
	v_pk_mul_f32 v[72:73], v[118:119], v[8:9] op_sel_hi:[0,1]
	v_pk_mul_f32 v[70:71], v[118:119], v[6:7] op_sel_hi:[0,1]
	v_pk_mul_f32 v[66:67], v[118:119], v[18:19] op_sel_hi:[0,1]
	v_bitop3_b32 v134, v114, v3, 32 bitop3:0x36
	v_bitop3_b32 v132, v114, v3, 64 bitop3:0x36
	v_cmp_gt_u32_e64 s[42:43], 32, v4
	v_add3_u32 v124, v22, s0, v0
	v_mov_b32_e32 v0, v1
	v_mov_b32_e32 v2, v1
	v_mov_b32_e32 v3, v1
	v_mov_b32_e32 v4, v1
	v_mov_b32_e32 v5, v1
	v_mov_b32_e32 v6, v1
	v_mov_b32_e32 v7, v1
	v_mov_b32_e32 v8, v1
	v_mov_b32_e32 v9, v1
	v_mov_b32_e32 v10, v1
	v_mov_b32_e32 v11, v1
	v_mov_b32_e32 v12, v1
	v_mov_b32_e32 v13, v1
	v_mov_b64_e32 v[64:65], v[14:15]
	v_mov_b64_e32 v[48:49], v[14:15]
	v_mov_b64_e32 v[32:33], v[14:15]
	v_pk_mul_f32 v[80:81], v[118:119], v[16:17] op_sel_hi:[0,1]
	v_mov_b64_e32 v[62:63], v[12:13]
	v_mov_b64_e32 v[60:61], v[10:11]
	v_mov_b64_e32 v[58:59], v[8:9]
	v_mov_b64_e32 v[56:57], v[6:7]
	v_mov_b64_e32 v[54:55], v[4:5]
	v_mov_b64_e32 v[52:53], v[2:3]
	v_mov_b64_e32 v[50:51], v[0:1]
	v_mov_b64_e32 v[46:47], v[12:13]
	v_mov_b64_e32 v[44:45], v[10:11]
	v_mov_b64_e32 v[42:43], v[8:9]
	v_mov_b64_e32 v[40:41], v[6:7]
	v_mov_b64_e32 v[38:39], v[4:5]
	v_mov_b64_e32 v[36:37], v[2:3]
	v_mov_b64_e32 v[34:35], v[0:1]
	v_mov_b64_e32 v[30:31], v[12:13]
	v_mov_b64_e32 v[28:29], v[10:11]
	v_mov_b64_e32 v[26:27], v[8:9]
	v_mov_b64_e32 v[24:25], v[6:7]
	v_mov_b64_e32 v[22:23], v[4:5]
	v_mov_b64_e32 v[20:21], v[2:3]
	v_mov_b64_e32 v[18:19], v[0:1]
	v_mov_b64_e32 v[16:17], v[14:15]
	v_mul_f32_e32 v129, 0x42000000, v118
	s_mov_b32 s28, 0
	v_lshlrev_b32_e32 v130, 8, v120
	v_lshl_add_u32 v115, v120, 2, s52
	s_add_i32 s29, 0, 0x20804
	v_mov_b64_e32 v[14:15], v[12:13]
	v_mov_b64_e32 v[12:13], v[10:11]
	v_mov_b64_e32 v[10:11], v[8:9]
	v_mov_b64_e32 v[8:9], v[6:7]
	v_mov_b64_e32 v[6:7], v[4:5]
	v_mov_b64_e32 v[4:5], v[2:3]
	v_mov_b64_e32 v[2:3], v[0:1]
	s_branch .LBB0_523

; __device__ __forceinline__ void qkt(f32x16& p0, f32x16& p1, const f32x16& init, const char* Kt, int r32, int hi, const char* qf  ) {
;     p0 = init; p1 = init;
;     const char* kb[4];
; #pragma unroll
;     for (int dd = 0; dd < 4; ++dd) kb[dd] = Kt + KSWZ(r32, (dd * 16 + hi * 8) * 2);
; #pragma unroll
;     for (int d0 = 0; d0 < 8; ++d0) { const char* a = kb[d0 & 3] + (d0 >> 2) * 128;
;         bf16x8 b0 = *reinterpret_cast<const bf16x8*>(a);
;         bf16x8 b1 = *reinterpret_cast<const bf16x8*>(a + 32 * 256);
;         const bf16x8 q = *reinterpret_cast<const bf16x8*>(qf + d0 * 1024);
;         p0 = __builtin_amdgcn_mfma_f32_32x32x16_bf16(b0, q, p0, 0, 0, 0);
;         p1 = __builtin_amdgcn_mfma_f32_32x32x16_bf16(b1, q, p1, 0, 0, 0); }
; template <int mode> __device__ __forceinline__ void attn_unit(const AttnArgs& A, const int b, const int h, const int sub, char* shm, const int wave_) {
;     ...
;     for (int t = 0; t < NT; ++t) {
;         const int buf = t & 1; const int kb = __builtin_amdgcn_readfirstlane(TL[t]);
;         const bool more = (t + 1 < NT);
;         if (more) { const int k1 = __builtin_amdgcn_readfirstlane(TL[t + 1]); TDMA(k1, buf ^ 1); }
;         bool act;
;         if (mode == 0) act = (kb <= qw0 + 31) && (kb + 63 >= qw0 - 128);
;         else if (mode == 1) act = (kb <= qw0 + 31);
;         else if (mode == 3) act = wvalid;
;         else act = (kb < qw0 + 32) && !wdone;
;         if (act) {
;             f32x16 p0, p1;
;             qkt(p0, p1, binit, K_lds + buf * SHM_T, r32, hi, qf);
.LBB0_523:
	s_add_i32 s0, s29, -4
	v_mov_b32_e32 v0, s0
	ds_read2_b32 v[82:83], v0 offset1:1
	v_mov_b32_e32 v0, v126
	v_mov_b32_e32 v84, v125
	s_waitcnt lgkmcnt(0)
	v_readfirstlane_b32 s0, v83
	s_mul_i32 s31, s0, 0x3000
	s_mul_hi_i32 s30, s0, 0x3000
	s_add_u32 s0, s15, s31
	s_addc_u32 s1, s22, s30
	s_add_u32 s34, s23, s31
	s_addc_u32 s35, s27, s30
	s_and_b32 s30, s28, 0x4000
	s_xor_b32 s31, s30, 0x4000
	s_add_i32 s31, s2, s31
	s_add_i32 m0, s31, 0x8000
	v_mov_b32_e32 v83, v127
	s_andn2_b64 vcc, exec, s[24:25]
	s_cmp_eq_u32 s28, 0
	s_cbranch_scc1 .Lgath_dma_done
	global_load_lds_dwordx4 v84, s[0:1]
	s_mov_b32 m0, s31
	s_nop 0
	global_load_lds_dwordx4 v0, s[34:35]
	v_mov_b32_e32 v0, v128
	s_add_i32 m0, s31, 0x8400
	s_nop 0
	global_load_lds_dwordx4 v83, s[0:1]
	s_add_i32 m0, s31, 0x400
	s_nop 0
	global_load_lds_dwordx4 v0, s[34:35]
.Lgath_dma_done:
	v_readfirstlane_b32 s0, v82
	v_cndmask_b32_e64 v0, 0, 1, s[24:25]
	v_cmp_ne_u32_e64 s[44:45], 1, v0
	s_cbranch_vccnz .LBB0_522
	s_add_i32 s1, s30, 0
	v_add3_u32 v0, s1, v135, v130
	v_add3_u32 v144, s1, v134, v130
	v_add3_u32 v145, s1, v132, v130
	v_add3_u32 v146, s1, v131, v130
	v_cvt_f32_i32_e32 v136, s0
	ds_read_b128 v[208:211], v0 offset:32768
	ds_read_b128 v[212:215], v0 offset:40960
	ds_read_b128 v[216:219], v123
	ds_read_b128 v[220:223], v144 offset:32768
	ds_read_b128 v[224:227], v144 offset:40960
	ds_read_b128 v[228:231], v123 offset:1024
	ds_read_b128 v[232:235], v145 offset:32768
	ds_read_b128 v[236:239], v145 offset:40960
	ds_read_b128 v[240:243], v123 offset:2048
	s_waitcnt lgkmcnt(6)
	v_mfma_f32_32x32x16_bf16 v[82:97], v[208:211], v[216:219], v[66:81]
	v_mfma_f32_32x32x16_bf16 v[98:113], v[212:215], v[216:219], v[66:81]
	ds_read_b128 v[208:211], v146 offset:32768
	ds_read_b128 v[212:215], v146 offset:40960
	ds_read_b128 v[216:219], v123 offset:3072
	s_waitcnt lgkmcnt(6)
	v_mfma_f32_32x32x16_bf16 v[82:97], v[220:223], v[228:231], v[82:97]
	v_mfma_f32_32x32x16_bf16 v[98:113], v[224:227], v[228:231], v[98:113]
	ds_read_b128 v[220:223], v0 offset:32896
	ds_read_b128 v[224:227], v0 offset:41088
	ds_read_b128 v[228:231], v123 offset:4096
	s_waitcnt lgkmcnt(6)
	v_mfma_f32_32x32x16_bf16 v[82:97], v[232:235], v[240:243], v[82:97]
	v_mfma_f32_32x32x16_bf16 v[98:113], v[236:239], v[240:243], v[98:113]
	ds_read_b128 v[232:235], v144 offset:32896
	ds_read_b128 v[236:239], v144 offset:41088
	ds_read_b128 v[240:243], v123 offset:5120
	s_waitcnt lgkmcnt(6)
	v_mfma_f32_32x32x16_bf16 v[82:97], v[208:211], v[216:219], v[82:97]
	v_mfma_f32_32x32x16_bf16 v[98:113], v[212:215], v[216:219], v[98:113]
	ds_read_b128 v[208:211], v145 offset:32896
	ds_read_b128 v[212:215], v145 offset:41088
	ds_read_b128 v[216:219], v123 offset:6144
	s_waitcnt lgkmcnt(6)
	v_mfma_f32_32x32x16_bf16 v[82:97], v[220:223], v[228:231], v[82:97]
	v_mfma_f32_32x32x16_bf16 v[98:113], v[224:227], v[228:231], v[98:113]
	ds_read_b128 v[220:223], v146 offset:41088
	ds_read_b128 v[224:227], v146 offset:32896
	ds_read_b128 v[228:231], v123 offset:7168
	s_waitcnt lgkmcnt(6)
	v_mfma_f32_32x32x16_bf16 v[82:97], v[232:235], v[240:243], v[82:97]
	v_mfma_f32_32x32x16_bf16 v[98:113], v[236:239], v[240:243], v[98:113]
	s_waitcnt lgkmcnt(3)
	v_mfma_f32_32x32x16_bf16 v[82:97], v[208:211], v[216:219], v[82:97]
	v_mfma_f32_32x32x16_bf16 v[98:113], v[212:215], v[216:219], v[98:113]
	s_waitcnt lgkmcnt(0)
; template <int mode> __device__ __forceinline__ void attn_unit(const AttnArgs& A, const int b, const int h, const int sub, char* shm, const int wave_) {
;     ...
;                 } else rowok = gvalid;
;                 const float tb = sl * (float)kb;
;                 float pm0 = p0[0], pm1 = p1[0];
; #pragma unroll
;                 for (int r = 1; r < 16; ++r) { pm0 = fmaxf(pm0, p0[r]); pm1 = fmaxf(pm1, p1[r]); }
;                 float pmax = fmaxf(pm0, pm1 + sl32);
;                 { auto rr = __builtin_amdgcn_permlane32_swap(__float_as_uint(pmax), __float_as_uint(pmax), false, false); pmax = fmaxf(__uint_as_float(rr[0]), __uint_as_float(rr[1])); }
;                 pmax = rowok ? pmax : NEG;
;                 const float m_loc = m_reg - tb;
;                 const float mn = fmaxf(m_loc, pmax); const float alpha = __builtin_amdgcn_exp2f(m_loc - mn); m_reg = mn + tb;
;                 const float ref0 = rowok ? mn : __builtin_inff(), ref1 = ref0 - sl32;
;                 float ps = 0.f;
; #pragma unroll
;                 for (int r = 0; r < 16; ++r) { p0[r] = __builtin_amdgcn_exp2f(p0[r] - ref0); p1[r] = __builtin_amdgcn_exp2f(p1[r] - ref1); ps += p0[r] + p1[r]; }
;                 { auto rr = __builtin_amdgcn_permlane32_swap(__float_as_uint(ps), __float_as_uint(ps), false, false); ps = __uint_as_float(rr[0]) + __uint_as_float(rr[1]); }
;                 l_reg = l_reg * alpha + ps;
;                 pack_p(p0, p1, pa0, pa1, pa2, pa3);
;                 if (__any(alpha < 1.f)) { if (hi == 0) al_l[r32] = alpha; asm volatile("s_waitcnt lgkmcnt(0)" ::: "memory");
	v_mfma_f32_32x32x16_bf16 v[98:113], v[220:223], v[228:231], v[98:113]
	v_mfma_f32_32x32x16_bf16 v[82:97], v[224:227], v[228:231], v[82:97]
	s_nop 1
	s_nop 9
	v_max_f32_e32 v0, v99, v99
	v_max_f32_e32 v137, v98, v98
	v_max_f32_e32 v0, v137, v0
	v_max3_f32 v0, v0, v100, v101
	v_max3_f32 v0, v0, v102, v103
	v_max3_f32 v0, v0, v104, v105
	v_max3_f32 v0, v0, v106, v107
	v_max3_f32 v137, v82, v83, v84
	v_max3_f32 v137, v137, v85, v86
	v_max3_f32 v137, v137, v87, v88
	v_max3_f32 v137, v137, v89, v90
	v_max3_f32 v0, v0, v108, v109
	v_max3_f32 v137, v137, v91, v92
	v_max3_f32 v0, v0, v110, v111
	v_max3_f32 v137, v137, v93, v94
	v_max3_f32 v0, v0, v112, v113
	v_max3_f32 v137, v137, v95, v96
	v_add_f32_e32 v0, v129, v0
	v_max3_f32 v0, v137, v97, v0
	v_mov_b32_e32 v137, v0
	s_nop 1
	v_permlane32_swap_b32_e32 v0, v137
	v_max_f32_e32 v137, v137, v137
	v_max_f32_e32 v0, v0, v0
	v_max_f32_e32 v0, v0, v137
	v_cndmask_b32_e64 v0, v206, v0, s[40:41]
	v_fma_f32 v137, -v118, v136, v116
	v_max_f32_e32 v116, v137, v0
	v_mov_b32_e32 v0, 0x7f800000
	v_cndmask_b32_e64 v142, v0, v116, s[40:41]
	v_sub_f32_e32 v143, v142, v129
	v_sub_f32_e32 v0, v82, v142
	v_exp_f32_e32 v144, v0
	v_sub_f32_e32 v0, v98, v143
	v_exp_f32_e32 v145, v0
	v_sub_f32_e32 v0, v83, v142
	v_exp_f32_e32 v82, v0
	v_sub_f32_e32 v0, v99, v143
	v_exp_f32_e32 v0, v0
	v_add_f32_e32 v83, v144, v145
	v_pk_add_f32 v[98:99], v[82:83], v[0:1]
	v_sub_f32_e32 v83, v84, v142
	v_sub_f32_e32 v84, v100, v143
	v_pk_add_f32 v[138:139], v[98:99], v[98:99] op_sel_hi:[0,1]
	v_exp_f32_e32 v83, v83
	v_exp_f32_e32 v146, v84
	v_sub_f32_e32 v84, v85, v142
	v_sub_f32_e32 v85, v101, v143
	v_exp_f32_e32 v84, v84
	v_exp_f32_e32 v138, v85
	v_add_f32_e32 v85, v83, v146
	v_cvt_pk_bf16_f32 v82, v144, v82
	v_cvt_pk_bf16_f32 v83, v83, v84
	v_pk_add_f32 v[98:99], v[84:85], v[138:139]
	v_sub_f32_e32 v85, v86, v142
	v_sub_f32_e32 v86, v102, v143
	v_pk_add_f32 v[100:101], v[98:99], v[98:99] op_sel_hi:[0,1]
	v_exp_f32_e32 v85, v85
	v_exp_f32_e32 v139, v86
	v_sub_f32_e32 v86, v87, v142
	v_sub_f32_e32 v87, v103, v143
	v_exp_f32_e32 v86, v86
	v_exp_f32_e32 v100, v87
	v_add_f32_e32 v87, v85, v139
	v_cvt_pk_bf16_f32 v84, v85, v86
	v_pk_add_f32 v[98:99], v[86:87], v[100:101]
	v_sub_f32_e32 v87, v88, v142
	v_sub_f32_e32 v88, v104, v143
	v_pk_add_f32 v[140:141], v[98:99], v[98:99] op_sel_hi:[0,1]
	v_exp_f32_e32 v87, v87
	v_exp_f32_e32 v101, v88
	v_sub_f32_e32 v88, v89, v142
	v_sub_f32_e32 v89, v105, v143
	v_exp_f32_e32 v88, v88
	v_exp_f32_e32 v140, v89
	v_add_f32_e32 v89, v87, v101
	v_cvt_pk_bf16_f32 v85, v87, v88
	v_permlane32_swap_b32_e32 v82, v84
	v_pk_add_f32 v[98:99], v[88:89], v[140:141]
	v_sub_f32_e32 v89, v90, v142
	v_sub_f32_e32 v90, v106, v143
	v_pk_add_f32 v[104:105], v[98:99], v[98:99] op_sel_hi:[0,1]
	v_exp_f32_e32 v89, v89
	v_exp_f32_e32 v103, v90
	v_sub_f32_e32 v90, v91, v142
	v_sub_f32_e32 v91, v107, v143
	v_exp_f32_e32 v90, v90
	v_exp_f32_e32 v104, v91
	v_add_f32_e32 v91, v89, v103
	v_cvt_pk_bf16_f32 v86, v89, v90
	v_permlane32_swap_b32_e32 v83, v85
	v_pk_add_f32 v[98:99], v[90:91], v[104:105]
	v_sub_f32_e32 v91, v92, v142
	v_sub_f32_e32 v92, v108, v143
	v_pk_add_f32 v[106:107], v[98:99], v[98:99] op_sel_hi:[0,1]
	v_exp_f32_e32 v91, v91
	v_exp_f32_e32 v105, v92
	v_sub_f32_e32 v92, v93, v142
	v_sub_f32_e32 v93, v109, v143
	v_exp_f32_e32 v92, v92
	v_exp_f32_e32 v106, v93
	v_add_f32_e32 v93, v91, v105
	v_cvt_pk_bf16_f32 v87, v91, v92
	v_pk_add_f32 v[98:99], v[92:93], v[106:107]
	v_sub_f32_e32 v93, v94, v142
	v_sub_f32_e32 v94, v110, v143
	v_pk_add_f32 v[108:109], v[98:99], v[98:99] op_sel_hi:[0,1]
	v_exp_f32_e32 v93, v93
	v_exp_f32_e32 v107, v94
	v_sub_f32_e32 v94, v95, v142
	v_sub_f32_e32 v95, v111, v143
	v_exp_f32_e32 v94, v94
	v_exp_f32_e32 v108, v95
	v_add_f32_e32 v95, v93, v107
	v_cvt_pk_bf16_f32 v88, v93, v94
	v_pk_add_f32 v[98:99], v[94:95], v[108:109]
	v_sub_f32_e32 v95, v96, v142
	v_sub_f32_e32 v96, v112, v143
	v_pk_add_f32 v[110:111], v[98:99], v[98:99] op_sel_hi:[0,1]
	v_exp_f32_e32 v95, v95
	v_exp_f32_e32 v109, v96
	v_sub_f32_e32 v96, v97, v142
	v_sub_f32_e32 v97, v113, v143
	v_exp_f32_e32 v96, v96
	v_exp_f32_e32 v110, v97
	v_sub_f32_e32 v97, v137, v116
	v_exp_f32_e32 v102, v97
	v_add_f32_e32 v97, v95, v109
	v_pk_add_f32 v[98:99], v[96:97], v[110:111]
	v_cvt_pk_bf16_f32 v89, v95, v96
	v_cvt_pk_bf16_f32 v90, v145, v0
	v_cvt_pk_bf16_f32 v91, v146, v138
	v_cvt_pk_bf16_f32 v92, v139, v100
	v_cvt_pk_bf16_f32 v93, v101, v140
	s_nop 0
	v_pk_add_f32 v[98:99], v[98:99], v[98:99] op_sel:[0,1] op_sel_hi:[1,0]
	v_cvt_pk_bf16_f32 v94, v103, v104
	v_cvt_pk_bf16_f32 v95, v105, v106
	v_cvt_pk_bf16_f32 v96, v107, v108
	v_cvt_pk_bf16_f32 v97, v109, v110
	v_permlane32_swap_b32_e32 v86, v88
	v_mov_b32_e32 v99, v98
	s_nop 1
	v_permlane32_swap_b32_e32 v98, v99
	v_permlane32_swap_b32_e32 v87, v89
	v_permlane32_swap_b32_e32 v90, v92
	v_permlane32_swap_b32_e32 v91, v93
	v_permlane32_swap_b32_e32 v94, v96
	v_permlane32_swap_b32_e32 v95, v97
	v_cmp_gt_f32_e32 vcc, 1.0, v102
	s_cbranch_vccz .LBB0_521
	s_and_saveexec_b64 s[0:1], s[42:43]
	s_cbranch_execz .LBB0_520
	ds_write_b32 v115, v102 offset:128
	s_branch .LBB0_520
